# ALIGN_EPI barrier moved after epilogue load issue in P12/P13 (leading half hides load latency)
# speedup vs baseline: 1.0226x; 1.0045x over previous
; #define PG8_BAR __builtin_amdgcn_s_barrier()
; template <class Epi, class Sched, bool ALIGN_EPI = false, bool SP2 = false>
; __device__ __forceinline__ void gemm_phase(PG8_LAS unsigned char* lds, const Geo geo, const Sched& S, const Epi& E, const int wave_) {
;     ...
;         if constexpr (ALIGN_EPI) { if (wr == 0) PG8_BAR; }
;     __device__ __forceinline__ void operator()(const f32x4 (&acc)[2][2][4][2], const Unit& u, int wr, int wc, int fr, int fq) const {
;         asm volatile("" : "+v"(fr), "+v"(fq));
;         const int e = blkE[u.z], c0 = u.pn * 128 + wc * 32 + 8 * fq, row0 = wr * 64 + fr;
;         const float* bg = bup + (size_t)e * 2 * FF + c0; const f32x4 g0 = *(const f32x4*)bg, g1 = *(const f32x4*)(bg + 4), l0 = *(const f32x4*)(bg + FF), l1 = *(const f32x4*)(bg + FF + 4);
;         float rsb[8];
; #pragma unroll
;         for (int q = 0; q < 8; ++q) rsb[q] = ssq[tokTab[u.pm * 256 + row0 + (q >> 2) * 128 + (q & 3) * 16]] * W8_INV;
; #pragma unroll
;         for (int ai = 0; ai < 2; ++ai)
; #pragma unroll
;             for (int m = 0; m < 4; ++m) { const int r = row0 + ai * 128 + m * 16; const float rs = rsb[ai * 4 + m];
;                 float a[8];
; #pragma unroll
;                 for (int j = 0; j < 8; ++j) { const float gb = j < 4 ? g0[j & 3] : g1[j & 3], lb = j < 4 ? l0[j & 3] : l1[j & 3];
;                     const float gl = fminf(acc[ai][0][m][j >> 2][j & 3] * rs + gb, 7.0f), ln = fminf(fmaxf(acc[ai][1][m][j >> 2][j & 3] * rs + lb, -7.0f), 7.0f);
;                     a[j] = gl * __builtin_amdgcn_rcpf(1.0f + __builtin_amdgcn_exp2f(-1.702f * 1.4426950408889634f * gl)) * (ln + 1.0f); }
;                 v2u w; w.x = pk4_fp8(a[0], a[1], a[2], a[3]); w.y = pk4_fp8(a[4], a[5], a[6], a[7]);
;                 *(v2u*)(ACT + ((size_t)u.z * 256 + r) * FF + c0) = w; }
.LBB0_1534:
	s_lshl_b32 s4, s40, 7
	v_mov_b32_e32 v2, v218
	v_mov_b32_e32 v3, v219
	s_or_b32 s4, s4, s89
	v_mov_b32_e32 v0, s35
	v_lshl_add_u32 v16, v3, 3, s4
	v_readlane_b32 s0, v254, 2
	v_readlane_b32 s4, v254, 6
	s_lshl_b32 s4, s65, 10
	v_add_u32_e32 v18, s88, v2
	s_add_i32 s4, s4, 0
	v_lshl_add_u32 v2, v18, 2, s4
	v_add_u32_e32 v9, 0x20400, v2
	ds_read2_b32 v[4:5], v9 offset1:16
	ds_read_b32 v0, v0
	v_readlane_b32 s1, v254, 3
	v_ashrrev_i32_e32 v17, 31, v16
	ds_read2_b32 v[20:21], v9 offset0:160 offset1:176
	s_waitcnt lgkmcnt(0)
	v_ashrrev_i32_e32 v11, 31, v4
	v_mov_b32_e32 v10, v4
	v_lshl_add_u64 v[10:11], v[10:11], 2, s[14:15]
	global_load_dword v19, v[10:11], off
	ds_read2_b32 v[10:11], v9 offset0:32 offset1:48
	v_ashrrev_i32_e32 v13, 31, v5
	v_mov_b32_e32 v12, v5
	v_lshl_add_u64 v[4:5], v[12:13], 2, s[14:15]
	global_load_dword v24, v[4:5], off
	s_waitcnt lgkmcnt(0)
	v_ashrrev_i32_e32 v5, 31, v10
	v_mov_b32_e32 v4, v10
	v_lshl_add_u64 v[4:5], v[4:5], 2, s[14:15]
	global_load_dword v25, v[4:5], off
	ds_read2_b32 v[4:5], v9 offset0:128 offset1:144
	v_ashrrev_i32_e32 v13, 31, v11
	v_mov_b32_e32 v12, v11
	v_lshl_add_u64 v[10:11], v[12:13], 2, s[14:15]
	v_ashrrev_i32_e32 v1, 31, v0
	global_load_dword v26, v[10:11], off
	s_waitcnt lgkmcnt(0)
	v_ashrrev_i32_e32 v11, 31, v4
	v_mov_b32_e32 v10, v4
	v_lshlrev_b64 v[0:1], 14, v[0:1]
	v_lshl_add_u64 v[10:11], v[10:11], 2, s[14:15]
	v_lshl_add_u64 v[0:1], s[0:1], 0, v[0:1]
	global_load_dword v27, v[10:11], off
	v_ashrrev_i32_e32 v11, 31, v5
	v_mov_b32_e32 v10, v5
	v_lshl_add_u64 v[6:7], v[16:17], 2, v[0:1]
	v_lshl_add_u64 v[4:5], v[10:11], 2, s[14:15]
	global_load_dwordx4 v[0:3], v[6:7], off
	global_load_dword v28, v[4:5], off
	v_ashrrev_i32_e32 v5, 31, v20
	v_mov_b32_e32 v4, v20
	v_add_co_u32_e32 v8, vcc, s56, v6
	v_lshl_add_u64 v[4:5], v[4:5], 2, s[14:15]
	global_load_dword v29, v[4:5], off
	v_addc_co_u32_e32 v9, vcc, 0, v7, vcc
	global_load_dwordx4 v[8:11], v[8:9], off
	s_nop 0
	global_load_dwordx4 v[12:15], v[6:7], off offset:16
	v_readlane_b32 s5, v254, 7
	s_mov_b64 s[4:5], 0x2000
	v_ashrrev_i32_e32 v23, 31, v21
	v_lshl_add_u64 v[4:5], v[6:7], 0, s[4:5]
	global_load_dwordx4 v[4:7], v[4:5], off offset:16
	v_mov_b32_e32 v22, v21
	v_lshl_add_u64 v[20:21], v[22:23], 2, s[14:15]
	global_load_dword v20, v[20:21], off
	s_ashr_i32 s39, s38, 31
	s_lshl_b64 s[4:5], s[38:39], 19
	s_add_u32 s4, s93, s4
	s_addc_u32 s5, s87, s5
	s_and_b64 vcc, exec, s[90:91]
	s_cbranch_vccz .Lepi12_nobar
	s_barrier
.Lepi12_nobar:
	v_readlane_b32 s0, v254, 10
	s_cmp_lg_u32 s65, s0
	v_readlane_b32 s2, v254, 4
	v_readlane_b32 s3, v254, 5
	v_readlane_b32 s6, v254, 8
	v_readlane_b32 s7, v254, 9
	s_waitcnt vmcnt(0)
	v_mul_f32_e32 v19, 0x3b800000, v19
	v_mul_f32_e32 v30, 0x3b800000, v24
	v_mul_f32_e32 v25, 0x3b800000, v25
	v_mul_f32_e32 v24, 0x3b800000, v26
	v_mul_f32_e32 v23, 0x3b800000, v27
	v_fma_f32 v26, v192, v19, v0
	v_mul_f32_e32 v22, 0x3b800000, v28
	v_fma_f32 v28, v193, v19, v1
	v_min_f32_e32 v26, 0x40e00000, v26
	v_min_f32_e32 v28, 0x40e00000, v28
	v_fma_f32 v31, v194, v19, v2
	v_mul_f32_e32 v34, 0xc01d265f, v26
	v_mul_f32_e32 v35, 0xc01d265f, v28
	v_min_f32_e32 v31, 0x40e00000, v31
	v_exp_f32_e32 v34, v34
	v_exp_f32_e32 v35, v35
	v_mul_f32_e32 v36, 0xc01d265f, v31
	v_fma_f32 v33, v195, v19, v3
	v_exp_f32_e32 v36, v36
	v_min_f32_e32 v33, 0x40e00000, v33
	v_mul_f32_e32 v37, 0xc01d265f, v33
	v_add_f32_e32 v34, 1.0, v34
	v_add_f32_e32 v35, 1.0, v35
	v_exp_f32_e32 v37, v37
	v_rcp_f32_e32 v34, v34
	v_rcp_f32_e32 v35, v35
	v_add_f32_e32 v36, 1.0, v36
	v_mul_f32_e32 v21, 0x3b800000, v29
	v_fma_f32 v27, v188, v19, v8
	v_fma_f32 v29, v189, v19, v9
	v_rcp_f32_e32 v36, v36
	v_med3_f32 v27, v27, s23, v236
	v_med3_f32 v29, v29, s23, v236
	v_fma_f32 v32, v190, v19, v10
	v_add_f32_e32 v27, 1.0, v27
	v_add_f32_e32 v29, 1.0, v29
	v_add_f32_e32 v37, 1.0, v37
	v_mul_f32_e32 v26, v26, v34
	v_mul_f32_e32 v28, v28, v35
	v_med3_f32 v32, v32, s23, v236
	v_mul_f32_e32 v26, v27, v26
	v_mul_f32_e32 v27, v29, v28
	v_rcp_f32_e32 v28, v37
	v_add_f32_e32 v32, 1.0, v32
	v_mul_f32_e32 v31, v31, v36
	v_mul_f32_e32 v29, v32, v31
	v_fma_f32 v32, v184, v19, v12
	v_min_f32_e32 v32, 0x40e00000, v32
	v_mul_f32_e32 v28, v33, v28
	v_mul_f32_e32 v33, 0xc01d265f, v32
	v_exp_f32_e32 v33, v33
	v_fma_f32 v34, v185, v19, v13
	v_min_f32_e32 v34, 0x40e00000, v34
	v_mul_f32_e32 v35, 0xc01d265f, v34
	v_add_f32_e32 v33, 1.0, v33
	v_rcp_f32_e32 v33, v33
	v_exp_f32_e32 v35, v35
	v_fma_f32 v31, v191, v19, v11
	v_fma_f32 v36, v187, v19, v15
	v_mul_f32_e32 v32, v32, v33
	v_add_f32_e32 v33, 1.0, v35
	v_rcp_f32_e32 v33, v33
	v_med3_f32 v31, v31, s23, v236
	v_min_f32_e32 v36, 0x40e00000, v36
	v_add_f32_e32 v31, 1.0, v31
	v_mul_f32_e32 v33, v34, v33
	v_fma_f32 v34, v186, v19, v14
	v_min_f32_e32 v34, 0x40e00000, v34
	v_mul_f32_e32 v35, 0xc01d265f, v34
	v_exp_f32_e32 v35, v35
	v_mul_f32_e32 v37, 0xc01d265f, v36
	v_mul_f32_e32 v28, v31, v28
	v_fma_f32 v31, v180, v19, v4
	v_add_f32_e32 v35, 1.0, v35
	v_rcp_f32_e32 v35, v35
	v_exp_f32_e32 v37, v37
	v_med3_f32 v31, v31, s23, v236
	v_add_f32_e32 v31, 1.0, v31
	v_mul_f32_e32 v31, v31, v32
	v_fma_f32 v32, v181, v19, v5
	v_med3_f32 v32, v32, s23, v236
	v_mul_f32_e32 v34, v34, v35
	v_add_f32_e32 v35, 1.0, v37
	v_add_f32_e32 v32, 1.0, v32
	v_rcp_f32_e32 v35, v35
	v_mul_f32_e32 v32, v32, v33
	v_fma_f32 v33, v182, v19, v6
	v_med3_f32 v33, v33, s23, v236
	v_fma_f32 v19, v183, v19, v7
	v_add_f32_e32 v33, 1.0, v33
	v_med3_f32 v19, v19, s23, v236
	v_mul_f32_e32 v33, v33, v34
	v_mul_f32_e32 v34, v36, v35
	v_add_f32_e32 v19, 1.0, v19
	v_mul_f32_e32 v19, v19, v34
	v_med3_f32 v34, v26, s24, v237
	v_med3_f32 v27, v27, s24, v237
	v_mov_b32_e32 v26, v65
;     __device__ __forceinline__ void operator()(const f32x4 (&acc)[2][2][4][2], const Unit& u, int wr, int wc, int fr, int fq) const {
;     ...
;             for (int m = 0; m < 4; ++m) { const int r = row0 + ai * 128 + m * 16; const float rs = rsb[ai * 4 + m];
;                 float a[8];
; #pragma unroll
;                 for (int j = 0; j < 8; ++j) { const float gb = j < 4 ? g0[j & 3] : g1[j & 3], lb = j < 4 ? l0[j & 3] : l1[j & 3];
;                     const float gl = fminf(acc[ai][0][m][j >> 2][j & 3] * rs + gb, 7.0f), ln = fminf(fmaxf(acc[ai][1][m][j >> 2][j & 3] * rs + lb, -7.0f), 7.0f);
;                     a[j] = gl * __builtin_amdgcn_rcpf(1.0f + __builtin_amdgcn_exp2f(-1.702f * 1.4426950408889634f * gl)) * (ln + 1.0f); }
;                 v2u w; w.x = pk4_fp8(a[0], a[1], a[2], a[3]); w.y = pk4_fp8(a[4], a[5], a[6], a[7]);
;                 *(v2u*)(ACT + ((size_t)u.z * 256 + r) * FF + c0) = w; }
	v_cvt_pk_fp8_f32 v26, v34, v27
	v_med3_f32 v31, v31, s24, v237
	v_med3_f32 v32, v32, s24, v237
	v_mov_b32_e32 v27, v65
	v_cvt_pk_fp8_f32 v27, v31, v32
	v_med3_f32 v29, v29, s24, v237
	v_med3_f32 v28, v28, s24, v237
	v_cvt_pk_fp8_f32 v26, v29, v28 op_sel:[0,0,1]
	v_med3_f32 v28, v33, s24, v237
	v_med3_f32 v19, v19, s24, v237
	v_cvt_pk_fp8_f32 v27, v28, v19 op_sel:[0,0,1]
	v_ashrrev_i32_e32 v19, 31, v18
	v_lshlrev_b64 v[18:19], 11, v[18:19]
	v_lshl_add_u64 v[18:19], s[4:5], 0, v[18:19]
	v_lshl_add_u64 v[16:17], v[18:19], 0, v[16:17]
	global_store_dwordx2 v[16:17], v[26:27], off
	v_fma_f32 v26, v177, v30, v1
	v_min_f32_e32 v26, 0x40e00000, v26
	v_fma_f32 v28, v176, v30, v0
	v_mul_f32_e32 v27, 0xc01d265f, v26
	v_min_f32_e32 v28, 0x40e00000, v28
	v_exp_f32_e32 v27, v27
	v_mul_f32_e32 v29, 0xc01d265f, v28
	v_exp_f32_e32 v29, v29
	v_fma_f32 v32, v169, v30, v13
	v_add_f32_e32 v27, 1.0, v27
	v_rcp_f32_e32 v27, v27
	v_add_f32_e32 v19, 1.0, v29
	v_rcp_f32_e32 v19, v19
	v_fma_f32 v29, v179, v30, v3
	v_mul_f32_e32 v26, v26, v27
	v_fma_f32 v27, v178, v30, v2
	v_min_f32_e32 v27, 0x40e00000, v27
	v_mul_f32_e32 v19, v28, v19
	v_mul_f32_e32 v28, 0xc01d265f, v27
	v_exp_f32_e32 v28, v28
	v_min_f32_e32 v29, 0x40e00000, v29
	v_mul_f32_e32 v31, 0xc01d265f, v29
	v_exp_f32_e32 v31, v31
	v_add_f32_e32 v28, 1.0, v28
	v_rcp_f32_e32 v28, v28
	v_min_f32_e32 v32, 0x40e00000, v32
	v_mul_f32_e32 v33, 0xc01d265f, v32
	v_exp_f32_e32 v33, v33
	v_mul_f32_e32 v27, v27, v28
	v_add_f32_e32 v28, 1.0, v31
	v_rcp_f32_e32 v28, v28
	v_fma_f32 v18, v172, v30, v8
	v_med3_f32 v18, v18, s23, v236
	v_add_f32_e32 v18, 1.0, v18
	v_mul_f32_e32 v28, v29, v28
	v_fma_f32 v29, v168, v30, v12
	v_min_f32_e32 v29, 0x40e00000, v29
	v_mul_f32_e32 v31, 0xc01d265f, v29
	v_exp_f32_e32 v31, v31
	v_mul_f32_e32 v18, v18, v19
	v_fma_f32 v19, v173, v30, v9
	v_med3_f32 v19, v19, s23, v236
	v_add_f32_e32 v31, 1.0, v31
	v_rcp_f32_e32 v31, v31
	v_add_f32_e32 v19, 1.0, v19
	v_mul_f32_e32 v19, v19, v26
	v_fma_f32 v26, v174, v30, v10
	v_mul_f32_e32 v29, v29, v31
	v_add_f32_e32 v31, 1.0, v33
	v_rcp_f32_e32 v31, v31
	v_med3_f32 v26, v26, s23, v236
	v_add_f32_e32 v26, 1.0, v26
	v_mul_f32_e32 v26, v26, v27
	v_mul_f32_e32 v31, v32, v31
	v_fma_f32 v32, v170, v30, v14
	v_min_f32_e32 v32, 0x40e00000, v32
	v_mul_f32_e32 v33, 0xc01d265f, v32
	v_exp_f32_e32 v33, v33
	v_fma_f32 v27, v175, v30, v11
	v_fma_f32 v34, v171, v30, v15
	v_med3_f32 v27, v27, s23, v236
	v_min_f32_e32 v34, 0x40e00000, v34
	v_add_f32_e32 v27, 1.0, v27
	v_add_f32_e32 v33, 1.0, v33
	v_mul_f32_e32 v35, 0xc01d265f, v34
	v_mul_f32_e32 v27, v27, v28
	v_fma_f32 v28, v164, v30, v4
	v_rcp_f32_e32 v33, v33
	v_exp_f32_e32 v35, v35
	v_med3_f32 v28, v28, s23, v236
	v_add_f32_e32 v28, 1.0, v28
	v_mul_f32_e32 v28, v28, v29
	v_fma_f32 v29, v165, v30, v5
	v_med3_f32 v29, v29, s23, v236
	v_mul_f32_e32 v32, v32, v33
	v_add_f32_e32 v33, 1.0, v35
	v_add_f32_e32 v29, 1.0, v29
	v_rcp_f32_e32 v33, v33
	v_mul_f32_e32 v29, v29, v31
	v_fma_f32 v31, v166, v30, v6
	v_med3_f32 v31, v31, s23, v236
	v_fma_f32 v30, v167, v30, v7
	v_add_f32_e32 v31, 1.0, v31
	v_med3_f32 v30, v30, s23, v236
	v_mul_f32_e32 v31, v31, v32
	v_mul_f32_e32 v32, v34, v33
	v_add_f32_e32 v30, 1.0, v30
	v_mul_f32_e32 v30, v30, v32
	v_med3_f32 v32, v18, s24, v237
	v_med3_f32 v19, v19, s24, v237
	v_mov_b32_e32 v18, v65
	v_cvt_pk_fp8_f32 v18, v32, v19
	v_med3_f32 v28, v28, s24, v237
	v_med3_f32 v29, v29, s24, v237
	v_mov_b32_e32 v19, v65
	v_cvt_pk_fp8_f32 v19, v28, v29
	v_med3_f32 v26, v26, s24, v237
	v_med3_f32 v27, v27, s24, v237
	v_cvt_pk_fp8_f32 v18, v26, v27 op_sel:[0,0,1]
	v_med3_f32 v26, v31, s24, v237
	v_med3_f32 v27, v30, s24, v237
	v_cvt_pk_fp8_f32 v19, v26, v27 op_sel:[0,0,1]
	v_fma_f32 v27, v160, v25, v0
	v_min_f32_e32 v28, 0x40e00000, v27
	v_add_co_u32_e32 v26, vcc, s73, v16
	v_mul_f32_e32 v27, 0xc01d265f, v28
	v_exp_f32_e32 v29, v27
	v_addc_co_u32_e32 v27, vcc, 0, v17, vcc
	global_store_dwordx2 v[26:27], v[18:19], off
	v_fma_f32 v26, v161, v25, v1
	v_min_f32_e32 v26, 0x40e00000, v26
	v_mul_f32_e32 v27, 0xc01d265f, v26
	v_exp_f32_e32 v27, v27
	v_add_f32_e32 v19, 1.0, v29
	v_rcp_f32_e32 v19, v19
	v_fma_f32 v29, v163, v25, v3
	v_add_f32_e32 v27, 1.0, v27
	v_rcp_f32_e32 v27, v27
	v_mul_f32_e32 v19, v28, v19
	v_min_f32_e32 v29, 0x40e00000, v29
	v_mul_f32_e32 v30, 0xc01d265f, v29
	v_mul_f32_e32 v26, v26, v27
	v_fma_f32 v27, v162, v25, v2
	v_min_f32_e32 v27, 0x40e00000, v27
	v_mul_f32_e32 v28, 0xc01d265f, v27
	v_exp_f32_e32 v28, v28
	v_exp_f32_e32 v30, v30
	v_fma_f32 v31, v153, v25, v13
	v_min_f32_e32 v31, 0x40e00000, v31
	v_add_f32_e32 v28, 1.0, v28
	v_rcp_f32_e32 v28, v28
	v_mul_f32_e32 v32, 0xc01d265f, v31
	v_exp_f32_e32 v32, v32
	v_fma_f32 v18, v156, v25, v8
	v_mul_f32_e32 v27, v27, v28
	v_add_f32_e32 v28, 1.0, v30
	v_rcp_f32_e32 v28, v28
	v_med3_f32 v18, v18, s23, v236
	v_add_f32_e32 v18, 1.0, v18
	v_mul_f32_e32 v18, v18, v19
	v_mul_f32_e32 v28, v29, v28
	v_fma_f32 v29, v152, v25, v12
	v_min_f32_e32 v29, 0x40e00000, v29
	v_mul_f32_e32 v30, 0xc01d265f, v29
	v_exp_f32_e32 v30, v30
	v_fma_f32 v19, v157, v25, v9
	v_med3_f32 v19, v19, s23, v236
	v_add_f32_e32 v19, 1.0, v19
	v_add_f32_e32 v30, 1.0, v30
	v_rcp_f32_e32 v30, v30
	v_mul_f32_e32 v19, v19, v26
	v_fma_f32 v26, v158, v25, v10
	v_med3_f32 v26, v26, s23, v236
	v_mul_f32_e32 v29, v29, v30
	v_add_f32_e32 v30, 1.0, v32
	v_rcp_f32_e32 v30, v30
	v_add_f32_e32 v26, 1.0, v26
	v_mul_f32_e32 v26, v26, v27
	v_fma_f32 v27, v159, v25, v11
	v_mul_f32_e32 v30, v31, v30
	v_fma_f32 v31, v154, v25, v14
	v_min_f32_e32 v31, 0x40e00000, v31
	v_mul_f32_e32 v32, 0xc01d265f, v31
	v_exp_f32_e32 v32, v32
	v_fma_f32 v33, v155, v25, v15
	v_med3_f32 v27, v27, s23, v236
;     __device__ __forceinline__ void operator()(const f32x4 (&acc)[2][2][4][2], const Unit& u, int wr, int wc, int fr, int fq) const {
;     ...
;             for (int m = 0; m < 4; ++m) { const int r = row0 + ai * 128 + m * 16; const float rs = rsb[ai * 4 + m];
;                 float a[8];
; #pragma unroll
;                 for (int j = 0; j < 8; ++j) { const float gb = j < 4 ? g0[j & 3] : g1[j & 3], lb = j < 4 ? l0[j & 3] : l1[j & 3];
;                     const float gl = fminf(acc[ai][0][m][j >> 2][j & 3] * rs + gb, 7.0f), ln = fminf(fmaxf(acc[ai][1][m][j >> 2][j & 3] * rs + lb, -7.0f), 7.0f);
;                     a[j] = gl * __builtin_amdgcn_rcpf(1.0f + __builtin_amdgcn_exp2f(-1.702f * 1.4426950408889634f * gl)) * (ln + 1.0f); }
;                 v2u w; w.x = pk4_fp8(a[0], a[1], a[2], a[3]); w.y = pk4_fp8(a[4], a[5], a[6], a[7]);
;                 *(v2u*)(ACT + ((size_t)u.z * 256 + r) * FF + c0) = w; }
	v_min_f32_e32 v33, 0x40e00000, v33
	v_add_f32_e32 v27, 1.0, v27
	v_add_f32_e32 v32, 1.0, v32
	v_mul_f32_e32 v34, 0xc01d265f, v33
	v_mul_f32_e32 v27, v27, v28
	v_fma_f32 v28, v148, v25, v4
	v_rcp_f32_e32 v32, v32
	v_exp_f32_e32 v34, v34
	v_med3_f32 v28, v28, s23, v236
	v_add_f32_e32 v28, 1.0, v28
	v_mul_f32_e32 v28, v28, v29
	v_fma_f32 v29, v149, v25, v5
	v_med3_f32 v29, v29, s23, v236
	v_mul_f32_e32 v31, v31, v32
	v_add_f32_e32 v32, 1.0, v34
	v_add_f32_e32 v29, 1.0, v29
	v_rcp_f32_e32 v32, v32
	v_mul_f32_e32 v29, v29, v30
	v_fma_f32 v30, v150, v25, v6
	v_med3_f32 v30, v30, s23, v236
	v_fma_f32 v25, v151, v25, v7
	v_add_f32_e32 v30, 1.0, v30
	v_med3_f32 v25, v25, s23, v236
	v_mul_f32_e32 v30, v30, v31
	v_mul_f32_e32 v31, v33, v32
	v_add_f32_e32 v25, 1.0, v25
	v_mul_f32_e32 v25, v25, v31
	v_med3_f32 v31, v18, s24, v237
	v_med3_f32 v19, v19, s24, v237
	v_mov_b32_e32 v18, v65
	v_cvt_pk_fp8_f32 v18, v31, v19
	v_med3_f32 v28, v28, s24, v237
	v_med3_f32 v29, v29, s24, v237
	v_mov_b32_e32 v19, v65
	v_cvt_pk_fp8_f32 v19, v28, v29
	v_med3_f32 v26, v26, s24, v237
	v_med3_f32 v27, v27, s24, v237
	v_cvt_pk_fp8_f32 v18, v26, v27 op_sel:[0,0,1]
	v_med3_f32 v26, v30, s24, v237
	v_med3_f32 v25, v25, s24, v237
	v_cvt_pk_fp8_f32 v19, v26, v25 op_sel:[0,0,1]
	v_fma_f32 v25, v144, v24, v0
	v_min_f32_e32 v25, 0x40e00000, v25
	v_mul_f32_e32 v27, 0xc01d265f, v25
	v_add_co_u32_e32 v26, vcc, s57, v16
	v_exp_f32_e32 v28, v27
	s_nop 0
	v_addc_co_u32_e32 v27, vcc, 0, v17, vcc
	global_store_dwordx2 v[26:27], v[18:19], off
	v_fma_f32 v26, v145, v24, v1
	v_min_f32_e32 v26, 0x40e00000, v26
	v_add_f32_e32 v19, 1.0, v28
	v_mul_f32_e32 v27, 0xc01d265f, v26
	v_rcp_f32_e32 v19, v19
	v_exp_f32_e32 v27, v27
	v_fma_f32 v28, v147, v24, v3
	v_min_f32_e32 v28, 0x40e00000, v28
	v_mul_f32_e32 v19, v25, v19
	v_add_f32_e32 v25, 1.0, v27
	v_rcp_f32_e32 v25, v25
	v_mul_f32_e32 v29, 0xc01d265f, v28
	v_exp_f32_e32 v29, v29
	v_fma_f32 v30, v137, v24, v13
	v_mul_f32_e32 v25, v26, v25
	v_fma_f32 v26, v146, v24, v2
	v_min_f32_e32 v26, 0x40e00000, v26
	v_mul_f32_e32 v27, 0xc01d265f, v26
	v_exp_f32_e32 v27, v27
	v_min_f32_e32 v30, 0x40e00000, v30
	v_mul_f32_e32 v31, 0xc01d265f, v30
	v_exp_f32_e32 v31, v31
	v_add_f32_e32 v27, 1.0, v27
	v_rcp_f32_e32 v27, v27
	v_fma_f32 v18, v140, v24, v8
	v_med3_f32 v18, v18, s23, v236
	v_add_f32_e32 v18, 1.0, v18
	v_mul_f32_e32 v26, v26, v27
	v_add_f32_e32 v27, 1.0, v29
	v_rcp_f32_e32 v27, v27
	v_mul_f32_e32 v18, v18, v19
	v_fma_f32 v19, v141, v24, v9
	v_med3_f32 v19, v19, s23, v236
	v_mul_f32_e32 v27, v28, v27
	v_fma_f32 v28, v136, v24, v12
	v_min_f32_e32 v28, 0x40e00000, v28
	v_mul_f32_e32 v29, 0xc01d265f, v28
	v_exp_f32_e32 v29, v29
	v_add_f32_e32 v19, 1.0, v19
	v_mul_f32_e32 v19, v19, v25
	v_fma_f32 v25, v142, v24, v10
	v_add_f32_e32 v29, 1.0, v29
	v_rcp_f32_e32 v29, v29
	v_med3_f32 v25, v25, s23, v236
	v_add_f32_e32 v25, 1.0, v25
	v_mul_f32_e32 v25, v25, v26
	v_mul_f32_e32 v28, v28, v29
	v_add_f32_e32 v29, 1.0, v31
	v_rcp_f32_e32 v29, v29
	v_fma_f32 v26, v143, v24, v11
	v_fma_f32 v32, v139, v24, v15
	v_med3_f32 v26, v26, s23, v236
	v_mul_f32_e32 v29, v30, v29
	v_fma_f32 v30, v138, v24, v14
	v_min_f32_e32 v30, 0x40e00000, v30
	v_mul_f32_e32 v31, 0xc01d265f, v30
	v_exp_f32_e32 v31, v31
	v_min_f32_e32 v32, 0x40e00000, v32
	v_add_f32_e32 v26, 1.0, v26
	v_mul_f32_e32 v33, 0xc01d265f, v32
	v_add_f32_e32 v31, 1.0, v31
	v_mul_f32_e32 v26, v26, v27
	v_fma_f32 v27, v132, v24, v4
	v_rcp_f32_e32 v31, v31
	v_exp_f32_e32 v33, v33
	v_med3_f32 v27, v27, s23, v236
	v_add_f32_e32 v27, 1.0, v27
	v_mul_f32_e32 v27, v27, v28
	v_fma_f32 v28, v133, v24, v5
	v_med3_f32 v28, v28, s23, v236
	v_mul_f32_e32 v30, v30, v31
	v_add_f32_e32 v31, 1.0, v33
	v_add_f32_e32 v28, 1.0, v28
	v_rcp_f32_e32 v31, v31
	v_mul_f32_e32 v28, v28, v29
	v_fma_f32 v29, v134, v24, v6
	v_med3_f32 v29, v29, s23, v236
	v_fma_f32 v24, v135, v24, v7
	v_add_f32_e32 v29, 1.0, v29
	v_med3_f32 v24, v24, s23, v236
	v_mul_f32_e32 v29, v29, v30
	v_mul_f32_e32 v30, v32, v31
	v_add_f32_e32 v24, 1.0, v24
	v_mul_f32_e32 v24, v24, v30
	v_med3_f32 v30, v18, s24, v237
	v_med3_f32 v19, v19, s24, v237
	v_mov_b32_e32 v18, v65
	v_cvt_pk_fp8_f32 v18, v30, v19
	v_med3_f32 v27, v27, s24, v237
	v_med3_f32 v28, v28, s24, v237
	v_mov_b32_e32 v19, v65
	v_cvt_pk_fp8_f32 v19, v27, v28
	v_med3_f32 v25, v25, s24, v237
	v_med3_f32 v26, v26, s24, v237
	v_cvt_pk_fp8_f32 v18, v25, v26 op_sel:[0,0,1]
	v_med3_f32 v25, v29, s24, v237
	v_med3_f32 v24, v24, s24, v237
	v_cvt_pk_fp8_f32 v19, v25, v24 op_sel:[0,0,1]
	v_fma_f32 v25, v128, v23, v0
	v_min_f32_e32 v26, 0x40e00000, v25
	v_add_co_u32_e32 v24, vcc, s69, v16
	v_mul_f32_e32 v25, 0xc01d265f, v26
	v_exp_f32_e32 v27, v25
	v_addc_co_u32_e32 v25, vcc, 0, v17, vcc
	global_store_dwordx2 v[24:25], v[18:19], off
	v_fma_f32 v24, v129, v23, v1
	v_min_f32_e32 v24, 0x40e00000, v24
	v_mul_f32_e32 v25, 0xc01d265f, v24
	v_exp_f32_e32 v25, v25
	v_add_f32_e32 v19, 1.0, v27
	v_rcp_f32_e32 v19, v19
	v_fma_f32 v27, v131, v23, v3
	v_add_f32_e32 v25, 1.0, v25
	v_rcp_f32_e32 v25, v25
	v_mul_f32_e32 v19, v26, v19
	v_min_f32_e32 v27, 0x40e00000, v27
	v_mul_f32_e32 v28, 0xc01d265f, v27
	v_mul_f32_e32 v24, v24, v25
	v_fma_f32 v25, v130, v23, v2
	v_min_f32_e32 v25, 0x40e00000, v25
	v_mul_f32_e32 v26, 0xc01d265f, v25
	v_exp_f32_e32 v26, v26
	v_exp_f32_e32 v28, v28
	v_fma_f32 v29, v121, v23, v13
	v_min_f32_e32 v29, 0x40e00000, v29
	v_add_f32_e32 v26, 1.0, v26
	v_rcp_f32_e32 v26, v26
	v_mul_f32_e32 v30, 0xc01d265f, v29
	v_exp_f32_e32 v30, v30
	v_fma_f32 v18, v124, v23, v8
	v_mul_f32_e32 v25, v25, v26
	v_add_f32_e32 v26, 1.0, v28
	v_rcp_f32_e32 v26, v26
	v_med3_f32 v18, v18, s23, v236
	v_add_f32_e32 v18, 1.0, v18
;     __device__ __forceinline__ void operator()(const f32x4 (&acc)[2][2][4][2], const Unit& u, int wr, int wc, int fr, int fq) const {
;     ...
; #pragma unroll
;         for (int ai = 0; ai < 2; ++ai)
; #pragma unroll
;             for (int m = 0; m < 4; ++m) { const int r = row0 + ai * 128 + m * 16; const float rs = rsb[ai * 4 + m];
;                 float a[8];
; #pragma unroll
;                 for (int j = 0; j < 8; ++j) { const float gb = j < 4 ? g0[j & 3] : g1[j & 3], lb = j < 4 ? l0[j & 3] : l1[j & 3];
;                     const float gl = fminf(acc[ai][0][m][j >> 2][j & 3] * rs + gb, 7.0f), ln = fminf(fmaxf(acc[ai][1][m][j >> 2][j & 3] * rs + lb, -7.0f), 7.0f);
;                     a[j] = gl * __builtin_amdgcn_rcpf(1.0f + __builtin_amdgcn_exp2f(-1.702f * 1.4426950408889634f * gl)) * (ln + 1.0f); }
;                 v2u w; w.x = pk4_fp8(a[0], a[1], a[2], a[3]); w.y = pk4_fp8(a[4], a[5], a[6], a[7]);
;                 *(v2u*)(ACT + ((size_t)u.z * 256 + r) * FF + c0) = w; }
	v_mul_f32_e32 v18, v18, v19
	v_mul_f32_e32 v26, v27, v26
	v_fma_f32 v27, v120, v23, v12
	v_min_f32_e32 v27, 0x40e00000, v27
	v_mul_f32_e32 v28, 0xc01d265f, v27
	v_exp_f32_e32 v28, v28
	v_fma_f32 v19, v125, v23, v9
	v_med3_f32 v19, v19, s23, v236
	v_add_f32_e32 v19, 1.0, v19
	v_add_f32_e32 v28, 1.0, v28
	v_rcp_f32_e32 v28, v28
	v_mul_f32_e32 v19, v19, v24
	v_fma_f32 v24, v126, v23, v10
	v_med3_f32 v24, v24, s23, v236
	v_mul_f32_e32 v27, v27, v28
	v_add_f32_e32 v28, 1.0, v30
	v_rcp_f32_e32 v28, v28
	v_add_f32_e32 v24, 1.0, v24
	v_mul_f32_e32 v24, v24, v25
	v_fma_f32 v25, v127, v23, v11
	v_mul_f32_e32 v28, v29, v28
	v_fma_f32 v29, v122, v23, v14
	v_min_f32_e32 v29, 0x40e00000, v29
	v_mul_f32_e32 v30, 0xc01d265f, v29
	v_exp_f32_e32 v30, v30
	v_fma_f32 v31, v123, v23, v15
	v_med3_f32 v25, v25, s23, v236
	v_min_f32_e32 v31, 0x40e00000, v31
	v_add_f32_e32 v25, 1.0, v25
	v_add_f32_e32 v30, 1.0, v30
	v_mul_f32_e32 v32, 0xc01d265f, v31
	v_mul_f32_e32 v25, v25, v26
	v_fma_f32 v26, v116, v23, v4
	v_rcp_f32_e32 v30, v30
	v_exp_f32_e32 v32, v32
	v_med3_f32 v26, v26, s23, v236
	v_add_f32_e32 v26, 1.0, v26
	v_mul_f32_e32 v26, v26, v27
	v_fma_f32 v27, v117, v23, v5
	v_med3_f32 v27, v27, s23, v236
	v_mul_f32_e32 v29, v29, v30
	v_add_f32_e32 v30, 1.0, v32
	v_add_f32_e32 v27, 1.0, v27
	v_rcp_f32_e32 v30, v30
	v_mul_f32_e32 v27, v27, v28
	v_fma_f32 v28, v118, v23, v6
	v_med3_f32 v28, v28, s23, v236
	v_fma_f32 v23, v119, v23, v7
	v_add_f32_e32 v28, 1.0, v28
	v_med3_f32 v23, v23, s23, v236
	v_mul_f32_e32 v28, v28, v29
	v_mul_f32_e32 v29, v31, v30
	v_add_f32_e32 v23, 1.0, v23
	v_mul_f32_e32 v23, v23, v29
	v_med3_f32 v29, v18, s24, v237
	v_med3_f32 v19, v19, s24, v237
	v_mov_b32_e32 v18, v65
	v_cvt_pk_fp8_f32 v18, v29, v19
	v_med3_f32 v26, v26, s24, v237
	v_med3_f32 v27, v27, s24, v237
	v_mov_b32_e32 v19, v65
	v_cvt_pk_fp8_f32 v19, v26, v27
	v_med3_f32 v24, v24, s24, v237
	v_med3_f32 v25, v25, s24, v237
	v_cvt_pk_fp8_f32 v18, v24, v25 op_sel:[0,0,1]
	v_med3_f32 v24, v28, s24, v237
	v_med3_f32 v23, v23, s24, v237
	v_cvt_pk_fp8_f32 v19, v24, v23 op_sel:[0,0,1]
	v_fma_f32 v23, v112, v22, v0
	v_min_f32_e32 v23, 0x40e00000, v23
	s_mov_b32 s4, 0x40000
	v_mul_f32_e32 v25, 0xc01d265f, v23
	v_add_co_u32_e32 v24, vcc, s4, v16
	v_exp_f32_e32 v26, v25
	s_nop 0
	v_addc_co_u32_e32 v25, vcc, 0, v17, vcc
	global_store_dwordx2 v[24:25], v[18:19], off
	v_fma_f32 v24, v113, v22, v1
	v_min_f32_e32 v24, 0x40e00000, v24
	v_add_f32_e32 v19, 1.0, v26
	v_mul_f32_e32 v25, 0xc01d265f, v24
	v_rcp_f32_e32 v19, v19
	v_exp_f32_e32 v25, v25
	v_fma_f32 v26, v115, v22, v3
	v_min_f32_e32 v26, 0x40e00000, v26
	v_mul_f32_e32 v19, v23, v19
	v_add_f32_e32 v23, 1.0, v25
	v_rcp_f32_e32 v23, v23
	v_mul_f32_e32 v27, 0xc01d265f, v26
	v_exp_f32_e32 v27, v27
	v_fma_f32 v28, v105, v22, v13
	v_mul_f32_e32 v23, v24, v23
	v_fma_f32 v24, v114, v22, v2
	v_min_f32_e32 v24, 0x40e00000, v24
	v_mul_f32_e32 v25, 0xc01d265f, v24
	v_exp_f32_e32 v25, v25
	v_min_f32_e32 v28, 0x40e00000, v28
	v_mul_f32_e32 v29, 0xc01d265f, v28
	v_exp_f32_e32 v29, v29
	v_add_f32_e32 v25, 1.0, v25
	v_rcp_f32_e32 v25, v25
	v_fma_f32 v18, v108, v22, v8
	v_med3_f32 v18, v18, s23, v236
	v_add_f32_e32 v18, 1.0, v18
	v_mul_f32_e32 v24, v24, v25
	v_add_f32_e32 v25, 1.0, v27
	v_rcp_f32_e32 v25, v25
	v_mul_f32_e32 v18, v18, v19
	v_fma_f32 v19, v109, v22, v9
	v_med3_f32 v19, v19, s23, v236
	v_mul_f32_e32 v25, v26, v25
	v_fma_f32 v26, v104, v22, v12
	v_min_f32_e32 v26, 0x40e00000, v26
	v_mul_f32_e32 v27, 0xc01d265f, v26
	v_exp_f32_e32 v27, v27
	v_add_f32_e32 v19, 1.0, v19
	v_mul_f32_e32 v19, v19, v23
	v_fma_f32 v23, v110, v22, v10
	v_add_f32_e32 v27, 1.0, v27
	v_rcp_f32_e32 v27, v27
	v_med3_f32 v23, v23, s23, v236
	v_add_f32_e32 v23, 1.0, v23
	v_mul_f32_e32 v23, v23, v24
	v_mul_f32_e32 v26, v26, v27
	v_add_f32_e32 v27, 1.0, v29
	v_rcp_f32_e32 v27, v27
	v_fma_f32 v24, v111, v22, v11
	v_fma_f32 v30, v107, v22, v15
	v_med3_f32 v24, v24, s23, v236
	v_mul_f32_e32 v27, v28, v27
	v_fma_f32 v28, v106, v22, v14
	v_min_f32_e32 v28, 0x40e00000, v28
	v_mul_f32_e32 v29, 0xc01d265f, v28
	v_exp_f32_e32 v29, v29
	v_min_f32_e32 v30, 0x40e00000, v30
	v_add_f32_e32 v24, 1.0, v24
	v_mul_f32_e32 v31, 0xc01d265f, v30
	v_add_f32_e32 v29, 1.0, v29
	v_mul_f32_e32 v24, v24, v25
	v_fma_f32 v25, v100, v22, v4
	v_rcp_f32_e32 v29, v29
	v_exp_f32_e32 v31, v31
	v_med3_f32 v25, v25, s23, v236
	v_add_f32_e32 v25, 1.0, v25
	v_mul_f32_e32 v25, v25, v26
	v_fma_f32 v26, v101, v22, v5
	v_med3_f32 v26, v26, s23, v236
	v_mul_f32_e32 v28, v28, v29
	v_add_f32_e32 v29, 1.0, v31
	v_add_f32_e32 v26, 1.0, v26
	v_rcp_f32_e32 v29, v29
	v_mul_f32_e32 v26, v26, v27
	v_fma_f32 v27, v102, v22, v6
	v_med3_f32 v27, v27, s23, v236
	v_fma_f32 v22, v103, v22, v7
	v_add_f32_e32 v27, 1.0, v27
	v_med3_f32 v22, v22, s23, v236
	v_mul_f32_e32 v27, v27, v28
	v_mul_f32_e32 v28, v30, v29
	v_add_f32_e32 v22, 1.0, v22
	v_mul_f32_e32 v22, v22, v28
	v_med3_f32 v28, v18, s24, v237
	v_med3_f32 v19, v19, s24, v237
	v_mov_b32_e32 v18, v65
	v_cvt_pk_fp8_f32 v18, v28, v19
	v_med3_f32 v25, v25, s24, v237
	v_med3_f32 v26, v26, s24, v237
	v_mov_b32_e32 v19, v65
	v_cvt_pk_fp8_f32 v19, v25, v26
	v_med3_f32 v23, v23, s24, v237
	v_med3_f32 v24, v24, s24, v237
	v_cvt_pk_fp8_f32 v18, v23, v24 op_sel:[0,0,1]
	v_med3_f32 v23, v27, s24, v237
	v_med3_f32 v22, v22, s24, v237
	v_cvt_pk_fp8_f32 v19, v23, v22 op_sel:[0,0,1]
	v_fma_f32 v23, v96, v21, v0
	s_mov_b32 s4, 0x48000
	v_min_f32_e32 v24, 0x40e00000, v23
	v_add_co_u32_e32 v22, vcc, s4, v16
	v_mul_f32_e32 v23, 0xc01d265f, v24
	v_exp_f32_e32 v25, v23
	v_addc_co_u32_e32 v23, vcc, 0, v17, vcc
	global_store_dwordx2 v[22:23], v[18:19], off
	v_fma_f32 v22, v97, v21, v1
	v_min_f32_e32 v22, 0x40e00000, v22
;     __device__ __forceinline__ void operator()(const f32x4 (&acc)[2][2][4][2], const Unit& u, int wr, int wc, int fr, int fq) const {
;     ...
; #pragma unroll
;         for (int ai = 0; ai < 2; ++ai)
; #pragma unroll
;             for (int m = 0; m < 4; ++m) { const int r = row0 + ai * 128 + m * 16; const float rs = rsb[ai * 4 + m];
;                 float a[8];
; #pragma unroll
;                 for (int j = 0; j < 8; ++j) { const float gb = j < 4 ? g0[j & 3] : g1[j & 3], lb = j < 4 ? l0[j & 3] : l1[j & 3];
;                     const float gl = fminf(acc[ai][0][m][j >> 2][j & 3] * rs + gb, 7.0f), ln = fminf(fmaxf(acc[ai][1][m][j >> 2][j & 3] * rs + lb, -7.0f), 7.0f);
;                     a[j] = gl * __builtin_amdgcn_rcpf(1.0f + __builtin_amdgcn_exp2f(-1.702f * 1.4426950408889634f * gl)) * (ln + 1.0f); }
;                 v2u w; w.x = pk4_fp8(a[0], a[1], a[2], a[3]); w.y = pk4_fp8(a[4], a[5], a[6], a[7]);
;                 *(v2u*)(ACT + ((size_t)u.z * 256 + r) * FF + c0) = w; }
;     }
;     __device__ __forceinline__ void done(const Unit& u) const { if (u.pm == (c & 7)) convert_share(); }
	v_mul_f32_e32 v23, 0xc01d265f, v22
	v_exp_f32_e32 v23, v23
	v_add_f32_e32 v19, 1.0, v25
	v_rcp_f32_e32 v19, v19
	v_fma_f32 v25, v99, v21, v3
	v_add_f32_e32 v23, 1.0, v23
	v_rcp_f32_e32 v23, v23
	v_mul_f32_e32 v19, v24, v19
	v_min_f32_e32 v25, 0x40e00000, v25
	v_mul_f32_e32 v26, 0xc01d265f, v25
	v_mul_f32_e32 v22, v22, v23
	v_fma_f32 v23, v98, v21, v2
	v_min_f32_e32 v23, 0x40e00000, v23
	v_mul_f32_e32 v24, 0xc01d265f, v23
	v_exp_f32_e32 v24, v24
	v_exp_f32_e32 v26, v26
	v_fma_f32 v27, v89, v21, v13
	v_min_f32_e32 v27, 0x40e00000, v27
	v_add_f32_e32 v24, 1.0, v24
	v_rcp_f32_e32 v24, v24
	v_mul_f32_e32 v28, 0xc01d265f, v27
	v_exp_f32_e32 v28, v28
	v_fma_f32 v18, v92, v21, v8
	v_mul_f32_e32 v23, v23, v24
	v_add_f32_e32 v24, 1.0, v26
	v_rcp_f32_e32 v24, v24
	v_med3_f32 v18, v18, s23, v236
	v_add_f32_e32 v18, 1.0, v18
	v_mul_f32_e32 v18, v18, v19
	v_mul_f32_e32 v24, v25, v24
	v_fma_f32 v25, v88, v21, v12
	v_min_f32_e32 v25, 0x40e00000, v25
	v_mul_f32_e32 v26, 0xc01d265f, v25
	v_exp_f32_e32 v26, v26
	v_fma_f32 v19, v93, v21, v9
	v_med3_f32 v19, v19, s23, v236
	v_add_f32_e32 v19, 1.0, v19
	v_add_f32_e32 v26, 1.0, v26
	v_rcp_f32_e32 v26, v26
	v_mul_f32_e32 v19, v19, v22
	v_fma_f32 v22, v94, v21, v10
	v_med3_f32 v22, v22, s23, v236
	v_mul_f32_e32 v25, v25, v26
	v_add_f32_e32 v26, 1.0, v28
	v_rcp_f32_e32 v26, v26
	v_add_f32_e32 v22, 1.0, v22
	v_mul_f32_e32 v22, v22, v23
	v_fma_f32 v23, v95, v21, v11
	v_mul_f32_e32 v26, v27, v26
	v_fma_f32 v27, v90, v21, v14
	v_min_f32_e32 v27, 0x40e00000, v27
	v_mul_f32_e32 v28, 0xc01d265f, v27
	v_exp_f32_e32 v28, v28
	v_fma_f32 v29, v91, v21, v15
	v_med3_f32 v23, v23, s23, v236
	v_min_f32_e32 v29, 0x40e00000, v29
	v_add_f32_e32 v23, 1.0, v23
	v_add_f32_e32 v28, 1.0, v28
	v_mul_f32_e32 v30, 0xc01d265f, v29
	v_mul_f32_e32 v23, v23, v24
	v_fma_f32 v24, v84, v21, v4
	v_rcp_f32_e32 v28, v28
	v_exp_f32_e32 v30, v30
	v_med3_f32 v24, v24, s23, v236
	v_add_f32_e32 v24, 1.0, v24
	v_mul_f32_e32 v24, v24, v25
	v_fma_f32 v25, v85, v21, v5
	v_med3_f32 v25, v25, s23, v236
	v_mul_f32_e32 v27, v27, v28
	v_add_f32_e32 v28, 1.0, v30
	v_add_f32_e32 v25, 1.0, v25
	v_rcp_f32_e32 v28, v28
	v_mul_f32_e32 v25, v25, v26
	v_fma_f32 v26, v86, v21, v6
	v_med3_f32 v26, v26, s23, v236
	v_fma_f32 v21, v87, v21, v7
	v_add_f32_e32 v26, 1.0, v26
	v_med3_f32 v21, v21, s23, v236
	v_mul_f32_e32 v26, v26, v27
	v_mul_f32_e32 v27, v29, v28
	v_add_f32_e32 v21, 1.0, v21
	v_mul_f32_e32 v21, v21, v27
	v_med3_f32 v27, v18, s24, v237
	v_med3_f32 v19, v19, s24, v237
	v_mov_b32_e32 v18, v65
	v_cvt_pk_fp8_f32 v18, v27, v19
	v_med3_f32 v24, v24, s24, v237
	v_med3_f32 v25, v25, s24, v237
	v_mov_b32_e32 v19, v65
	v_cvt_pk_fp8_f32 v19, v24, v25
	v_mul_f32_e32 v20, 0x3b800000, v20
	v_med3_f32 v22, v22, s24, v237
	v_med3_f32 v23, v23, s24, v237
	v_fma_f32 v14, v74, v20, v14
	v_cvt_pk_fp8_f32 v18, v22, v23 op_sel:[0,0,1]
	v_med3_f32 v22, v26, s24, v237
	v_med3_f32 v21, v21, s24, v237
	v_min_f32_e32 v14, 0x40e00000, v14
	v_cvt_pk_fp8_f32 v19, v22, v21 op_sel:[0,0,1]
	v_mul_f32_e32 v21, 0xc01d265f, v14
	v_exp_f32_e32 v21, v21
	s_mov_b32 s4, 0x50000
	v_add_co_u32_e32 v22, vcc, s4, v16
	v_fma_f32 v13, v73, v20, v13
	s_nop 0
	v_addc_co_u32_e32 v23, vcc, 0, v17, vcc
	global_store_dwordx2 v[22:23], v[18:19], off
	v_add_f32_e32 v18, 1.0, v21
	v_rcp_f32_e32 v18, v18
	v_min_f32_e32 v13, 0x40e00000, v13
	v_fma_f32 v6, v70, v20, v6
	v_med3_f32 v6, v6, s23, v236
	v_mul_f32_e32 v14, v14, v18
	v_mul_f32_e32 v18, 0xc01d265f, v13
	v_exp_f32_e32 v18, v18
	v_add_f32_e32 v6, 1.0, v6
	v_fma_f32 v12, v72, v20, v12
	v_mul_f32_e32 v6, v6, v14
	v_add_f32_e32 v14, 1.0, v18
	v_min_f32_e32 v12, 0x40e00000, v12
	v_rcp_f32_e32 v14, v14
	v_mul_f32_e32 v18, 0xc01d265f, v12
	v_exp_f32_e32 v18, v18
	v_fma_f32 v5, v69, v20, v5
	v_med3_f32 v5, v5, s23, v236
	v_add_f32_e32 v5, 1.0, v5
	v_mul_f32_e32 v13, v13, v14
	v_mul_f32_e32 v5, v5, v13
	v_add_f32_e32 v13, 1.0, v18
	v_rcp_f32_e32 v13, v13
	v_fma_f32 v3, v83, v20, v3
	v_min_f32_e32 v3, 0x40e00000, v3
	v_fma_f32 v4, v68, v20, v4
	v_mul_f32_e32 v12, v12, v13
	v_mul_f32_e32 v13, 0xc01d265f, v3
	v_exp_f32_e32 v13, v13
	v_med3_f32 v4, v4, s23, v236
	v_add_f32_e32 v4, 1.0, v4
	v_fma_f32 v2, v82, v20, v2
	v_mul_f32_e32 v4, v4, v12
	v_add_f32_e32 v12, 1.0, v13
	v_min_f32_e32 v2, 0x40e00000, v2
	v_rcp_f32_e32 v12, v12
	v_mul_f32_e32 v13, 0xc01d265f, v2
	v_exp_f32_e32 v13, v13
	v_fma_f32 v11, v79, v20, v11
	v_med3_f32 v11, v11, s23, v236
	v_add_f32_e32 v11, 1.0, v11
	v_mul_f32_e32 v3, v3, v12
	v_mul_f32_e32 v3, v11, v3
	v_add_f32_e32 v11, 1.0, v13
	v_rcp_f32_e32 v11, v11
	v_fma_f32 v10, v78, v20, v10
	v_med3_f32 v10, v10, s23, v236
	v_fma_f32 v1, v81, v20, v1
	v_add_f32_e32 v10, 1.0, v10
	v_mul_f32_e32 v2, v2, v11
	v_min_f32_e32 v1, 0x40e00000, v1
	v_mul_f32_e32 v2, v10, v2
	v_mul_f32_e32 v10, 0xc01d265f, v1
	v_exp_f32_e32 v10, v10
	v_fmac_f32_e32 v0, v80, v20
	v_min_f32_e32 v0, 0x40e00000, v0
	v_mul_f32_e32 v11, 0xc01d265f, v0
	v_add_f32_e32 v10, 1.0, v10
	v_rcp_f32_e32 v10, v10
	v_exp_f32_e32 v11, v11
	v_fma_f32 v9, v77, v20, v9
	v_med3_f32 v9, v9, s23, v236
	v_fmac_f32_e32 v15, v75, v20
	v_add_f32_e32 v9, 1.0, v9
	v_mul_f32_e32 v1, v1, v10
	v_min_f32_e32 v10, 0x40e00000, v15
	v_mul_f32_e32 v1, v9, v1
	v_add_f32_e32 v9, 1.0, v11
	v_mul_f32_e32 v11, 0xc01d265f, v10
	v_rcp_f32_e32 v9, v9
	v_exp_f32_e32 v11, v11
	v_fmac_f32_e32 v8, v76, v20
	v_med3_f32 v8, v8, s23, v236
	v_mul_f32_e32 v0, v0, v9
	v_add_f32_e32 v9, 1.0, v11
	v_rcp_f32_e32 v9, v9
	v_fmac_f32_e32 v7, v71, v20
	v_add_f32_e32 v8, 1.0, v8
	v_med3_f32 v7, v7, s23, v236
	v_mul_f32_e32 v0, v8, v0
	v_mul_f32_e32 v8, v10, v9
	v_add_f32_e32 v7, 1.0, v7
	v_mul_f32_e32 v7, v7, v8
	v_med3_f32 v8, v0, s24, v237
	v_med3_f32 v1, v1, s24, v237
	v_mov_b32_e32 v0, v65
	v_cvt_pk_fp8_f32 v0, v8, v1
	v_med3_f32 v4, v4, s24, v237
	v_med3_f32 v5, v5, s24, v237
	v_mov_b32_e32 v1, v65
	v_cvt_pk_fp8_f32 v1, v4, v5
	v_med3_f32 v2, v2, s24, v237
	v_med3_f32 v3, v3, s24, v237
	v_cvt_pk_fp8_f32 v0, v2, v3 op_sel:[0,0,1]
	v_med3_f32 v2, v6, s24, v237
	v_med3_f32 v3, v7, s24, v237
	v_cvt_pk_fp8_f32 v1, v2, v3 op_sel:[0,0,1]
	v_add_co_u32_e32 v2, vcc, 0x58000, v16
	s_nop 1
	v_addc_co_u32_e32 v3, vcc, 0, v17, vcc
	global_store_dwordx2 v[2:3], v[0:1], off
	s_cbranch_scc1 .LBB0_1541
; __device__ __forceinline__ int lane_id_now() { unsigned z = 0u; asm volatile("" : "+v"(z)); return (int)__builtin_amdgcn_mbcnt_hi(~0u, __builtin_amdgcn_mbcnt_lo(~0u, z)); }
; #define GAS __attribute__((address_space(1)))
; template <bool GAIN, bool NT = false> __device__ __forceinline__ void titem8_load(const TItem& d, int lane, f32x4 (&r)[16], f32x4 (&g)[4]) {
;     const int q = lane & 7, kg = lane >> 3; const unsigned lo = (unsigned)((16 * kg) * d.N + 4 * q) * 4u;
;     const GAS char* base = (const GAS char*)d.src;
; #pragma unroll
;     for (int j = 0; j < 16; ++j) { const GAS f32x4* p = (const GAS f32x4*)(base + (size_t)j * (size_t)d.N * 4 + lo); r[j] = NT ? __builtin_nontemporal_load(p) : *p; }
;     if constexpr (GAIN) { const GAS char* gb = (const GAS char*)d.gain; const unsigned go = (unsigned)(16 * kg) * 4u;
; #pragma unroll
;         for (int j4 = 0; j4 < 4; ++j4) g[j4] = *(const GAS f32x4*)(gb + 16 * j4 + go); }
;     asm volatile("" ::: "memory"); __builtin_amdgcn_sched_barrier(0);
; }
;     __device__ __forceinline__ void convert_share() const {
;         const int lane = lane_id_now(), gw = c * NWAVES + wave, NGW = G * NWAVES;
;         constexpr int NIT = E * (FF / 128) * (D / 32);
;         TSTREAM(NIT, dec_dn, TI8L_NT, TI8S_NT);
	v_readlane_b32 s0, v254, 26
	v_readlane_b32 s1, v254, 27
	v_mov_b32_e32 v0, v65
	s_andn2_b64 vcc, exec, s[0:1]
	s_cbranch_vccnz .LBB0_1541
	v_mbcnt_lo_u32_b32 v0, -1, v0
	v_mbcnt_hi_u32_b32 v66, -1, v0
	v_lshlrev_b32_e32 v1, 2, v66
	v_lshlrev_b32_e32 v0, 12, v66
	v_and_b32_e32 v67, 28, v1
	s_mov_b32 s4, 0x3fff8000
	v_and_or_b32 v0, v0, s4, v67
	v_readlane_b32 s4, v255, 5
	v_lshlrev_b32_e32 v64, 2, v0
	v_readlane_b32 s5, v255, 6
	s_mov_b64 s[46:47], s[90:91]
	s_mov_b32 s2, s89
	v_lshl_add_u64 v[0:1], s[4:5], 0, v[64:65]
	v_add_co_u32_e32 v2, vcc, 0x2000, v0
	s_mov_b32 s1, s88
	s_nop 0
	v_addc_co_u32_e32 v3, vcc, 0, v1, vcc
	global_load_dwordx4 v[8:11], v64, s[4:5] nt
	global_load_dwordx4 v[4:7], v[2:3], off nt
	v_add_co_u32_e32 v2, vcc, 0x4000, v0
	s_mov_b32 s0, s87
	s_nop 0
	v_addc_co_u32_e32 v3, vcc, 0, v1, vcc
	v_add_co_u32_e32 v12, vcc, 0x6000, v0
	v_lshlrev_b32_e32 v66, 1, v66
	s_nop 0
	v_addc_co_u32_e32 v13, vcc, 0, v1, vcc
	global_load_dwordx4 v[16:19], v[2:3], off nt
	s_nop 0
	global_load_dwordx4 v[12:15], v[12:13], off nt
	v_add_co_u32_e32 v2, vcc, 0x8000, v0
	s_nop 1
	v_addc_co_u32_e32 v3, vcc, 0, v1, vcc
	v_add_co_u32_e32 v20, vcc, 0xa000, v0
	s_nop 1
	v_addc_co_u32_e32 v21, vcc, 0, v1, vcc
	global_load_dwordx4 v[24:27], v[2:3], off nt
	s_nop 0
	global_load_dwordx4 v[20:23], v[20:21], off nt
	v_add_co_u32_e32 v2, vcc, 0xc000, v0
	s_nop 1
	v_addc_co_u32_e32 v3, vcc, 0, v1, vcc
	v_add_co_u32_e32 v28, vcc, 0xe000, v0
	s_nop 1
	v_addc_co_u32_e32 v29, vcc, 0, v1, vcc
	global_load_dwordx4 v[32:35], v[2:3], off nt
	s_nop 0
	global_load_dwordx4 v[28:31], v[28:29], off nt
	v_add_co_u32_e32 v2, vcc, s57, v0
	s_nop 1
	v_addc_co_u32_e32 v3, vcc, 0, v1, vcc
	v_add_co_u32_e32 v36, vcc, s58, v0
	s_nop 1
	v_addc_co_u32_e32 v37, vcc, 0, v1, vcc
	global_load_dwordx4 v[40:43], v[2:3], off nt
	s_nop 0
	global_load_dwordx4 v[36:39], v[36:37], off nt
	v_add_co_u32_e32 v2, vcc, s59, v0
	s_nop 1
	v_addc_co_u32_e32 v3, vcc, 0, v1, vcc
	v_add_co_u32_e32 v44, vcc, s60, v0
	s_nop 1
	v_addc_co_u32_e32 v45, vcc, 0, v1, vcc
	global_load_dwordx4 v[48:51], v[2:3], off nt
	s_nop 0
	global_load_dwordx4 v[44:47], v[44:45], off nt
	v_add_co_u32_e32 v2, vcc, s69, v0
	s_nop 1
	v_addc_co_u32_e32 v3, vcc, 0, v1, vcc
	v_add_co_u32_e32 v52, vcc, s71, v0
	s_nop 1
	v_addc_co_u32_e32 v53, vcc, 0, v1, vcc
	global_load_dwordx4 v[56:59], v[2:3], off nt
	s_nop 0
	global_load_dwordx4 v[52:55], v[52:53], off nt
	v_add_co_u32_e32 v2, vcc, 0x1c000, v0
	s_nop 1
	v_addc_co_u32_e32 v3, vcc, 0, v1, vcc
	v_add_co_u32_e32 v0, vcc, 0x1e000, v0
	s_nop 1
	v_addc_co_u32_e32 v1, vcc, 0, v1, vcc
	global_load_dwordx4 v[60:63], v[2:3], off nt
	s_nop 0
	global_load_dwordx4 v[0:3], v[0:1], off nt
	v_and_b32_e32 v66, -16, v66
	v_readlane_b32 s4, v255, 9
	v_readlane_b32 s6, v255, 7
	v_lshl_add_u32 v130, v67, 11, v66
	v_readlane_b32 s5, v255, 10
	v_readlane_b32 s7, v255, 8
	s_waitcnt vmcnt(0)
	v_mov_b64_e32 v[68:69], v[2:3]
	v_mov_b64_e32 v[128:129], v[62:63]
	v_mov_b64_e32 v[120:121], v[54:55]
	v_mov_b64_e32 v[124:125], v[58:59]
	v_mov_b64_e32 v[112:113], v[46:47]
	v_mov_b64_e32 v[116:117], v[50:51]
	v_mov_b64_e32 v[104:105], v[38:39]
	v_mov_b64_e32 v[108:109], v[42:43]
	v_mov_b64_e32 v[96:97], v[30:31]
	v_mov_b64_e32 v[100:101], v[34:35]
	v_mov_b64_e32 v[88:89], v[22:23]
	v_mov_b64_e32 v[92:93], v[26:27]
	v_mov_b64_e32 v[80:81], v[14:15]
	v_mov_b64_e32 v[84:85], v[18:19]
	v_mov_b64_e32 v[72:73], v[6:7]
	v_mov_b64_e32 v[76:77], v[10:11]
	v_mov_b32_e32 v131, v65
	s_andn2_b64 vcc, exec, s[4:5]
	s_mov_b64 s[4:5], s[6:7]
	v_readlane_b32 s35, v255, 4
	v_mov_b64_e32 v[66:67], v[0:1]
	v_mov_b64_e32 v[126:127], v[60:61]
	v_mov_b64_e32 v[118:119], v[52:53]
	v_mov_b64_e32 v[122:123], v[56:57]
	v_mov_b64_e32 v[110:111], v[44:45]
	v_mov_b64_e32 v[114:115], v[48:49]
	v_mov_b64_e32 v[102:103], v[36:37]
	v_mov_b64_e32 v[106:107], v[40:41]
	v_mov_b64_e32 v[94:95], v[28:29]
	v_mov_b64_e32 v[98:99], v[32:33]
	v_mov_b64_e32 v[86:87], v[20:21]
	v_mov_b64_e32 v[90:91], v[24:25]
	v_mov_b64_e32 v[78:79], v[12:13]
	v_mov_b64_e32 v[82:83], v[16:17]
	v_mov_b64_e32 v[70:71], v[4:5]
	v_mov_b64_e32 v[74:75], v[8:9]
	s_cbranch_vccz .LBB0_1538
	s_branch .LBB0_1540

; #define PG8_BAR __builtin_amdgcn_s_barrier()
; template <class Epi, class Sched, bool ALIGN_EPI = false, bool SP2 = false>
; __device__ __forceinline__ void gemm_phase(PG8_LAS unsigned char* lds, const Geo geo, const Sched& S, const Epi& E, const int wave_) {
;     ...
;         if constexpr (ALIGN_EPI) { if (wr == 0) PG8_BAR; }
;     __device__ __forceinline__ void operator()(const f32x4 (&acc)[2][2][4][2], const Unit& u, int wr, int wc, int fr, int fq) const {
;         const int e = blkE[u.z], row0 = wr * 64 + fr;
;         f32x4 bq[2][2];
; #pragma unroll
;         for (int bj = 0; bj < 2; ++bj) { const int c0 = u.pn * 256 + bj * 128 + wc * 32 + 8 * fq; bq[bj][0] = *(const f32x4*)(bdn + (size_t)e * D + c0); bq[bj][1] = *(const f32x4*)(bdn + (size_t)e * D + c0 + 4); }
; #pragma unroll
;         for (int bj = 0; bj < 2; ++bj) { const int c0 = u.pn * 256 + bj * 128 + wc * 32 + 8 * fq; const f32x4 b0 = bq[bj][0] * Y8_SCALE, b1 = bq[bj][1] * Y8_SCALE;
; #pragma unroll
;             for (int ai = 0; ai < 2; ++ai)
; #pragma unroll
;                 for (int m = 0; m < 4; ++m) { const int r = row0 + ai * 128 + m * 16; const f32x4 v0 = acc[ai][bj][m][0] * (W8_INV * Y8_SCALE) + b0, v1 = acc[ai][bj][m][1] * (W8_INV * Y8_SCALE) + b1; v2u w;
;                     w.x = pk4_fp8(v0[0], v0[1], v0[2], v0[3]); w.y = pk4_fp8(v1[0], v1[1], v1[2], v1[3]);
;                     *(v2u*)(YK + ((size_t)u.z * 256 + r) * D + c0) = w; } }
.LBB0_1623:
	v_mov_b32_e32 v0, s19
	ds_read_b32 v2, v0
	v_readlane_b32 s56, v254, 2
	v_lshl_or_b32 v0, s28, 8, v246
	v_readlane_b32 s60, v254, 6
	v_readlane_b32 s61, v254, 7
	s_waitcnt lgkmcnt(0)
	v_ashrrev_i32_e32 v3, 31, v2
	v_lshlrev_b64 v[2:3], 13, v[2:3]
	v_ashrrev_i32_e32 v1, 31, v0
	v_lshl_add_u64 v[2:3], s[60:61], 0, v[2:3]
	v_lshl_add_u64 v[2:3], v[0:1], 2, v[2:3]
	global_load_dwordx4 v[10:13], v[2:3], off
	global_load_dwordx4 v[14:17], v[2:3], off offset:16
	global_load_dwordx4 v[18:21], v[2:3], off offset:528
	global_load_dwordx4 v[22:25], v[2:3], off offset:512
	v_mov_b32_e32 v26, 0
	v_mov_b32_e32 v27, 0
	v_mov_b32_e32 v28, 0
	v_mov_b32_e32 v29, 0
	v_mov_b32_e32 v30, 0
	v_mov_b32_e32 v31, 0
	s_ashr_i32 s27, s26, 31
	v_mov_b32_e32 v32, 0
	v_mov_b32_e32 v33, 0
	s_lshl_b64 s[4:5], s[26:27], 19
	s_add_u32 s4, s45, s4
	s_addc_u32 s5, s46, s5
	v_lshl_add_u64 v[4:5], s[4:5], 0, v[204:205]
	v_lshl_add_u64 v[6:7], s[4:5], 0, v[206:207]
	v_lshl_add_u64 v[8:9], s[4:5], 0, v[208:209]
	v_lshl_add_u64 v[4:5], v[4:5], 0, v[0:1]
	v_lshl_add_u64 v[6:7], v[6:7], 0, v[0:1]
	v_lshl_add_u64 v[8:9], v[8:9], 0, v[0:1]
	v_lshl_add_u64 v[34:35], s[4:5], 0, v[210:211]
	s_and_b64 vcc, exec, s[12:13]
	s_cbranch_vccz .Lepi13_nobar
	s_barrier
.Lepi13_nobar:
	s_and_b64 vcc, exec, s[0:1]
	s_mov_b64 s[0:1], -1
	v_readlane_b32 s57, v254, 3
	v_readlane_b32 s58, v254, 4
	v_readlane_b32 s59, v254, 5
	v_readlane_b32 s62, v254, 8
	v_readlane_b32 s63, v254, 9
	s_waitcnt vmcnt(0)
	v_pk_mul_f32 v[38:39], v[10:11], s[14:15] op_sel_hi:[1,0]
	v_pk_mul_f32 v[14:15], v[14:15], s[14:15] op_sel_hi:[1,0]
	v_pk_fma_f32 v[10:11], v[192:193], s[16:17], v[38:39] op_sel_hi:[1,0,1]
	v_pk_fma_f32 v[40:41], v[188:189], s[16:17], v[14:15] op_sel_hi:[1,0,1]
	v_pk_fma_f32 v[44:45], v[184:185], s[16:17], v[38:39] op_sel_hi:[1,0,1]
	v_pk_fma_f32 v[48:49], v[180:181], s[16:17], v[14:15] op_sel_hi:[1,0,1]
	v_med3_f32 v10, v10, s55, v248
	v_med3_f32 v11, v11, s55, v248
	v_med3_f32 v40, v40, s55, v248
	v_med3_f32 v41, v41, s55, v248
	v_pk_fma_f32 v[52:53], v[176:177], s[16:17], v[38:39] op_sel_hi:[1,0,1]
	v_pk_fma_f32 v[56:57], v[172:173], s[16:17], v[14:15] op_sel_hi:[1,0,1]
	v_med3_f32 v44, v44, s55, v248
	v_med3_f32 v45, v45, s55, v248
	v_med3_f32 v48, v48, s55, v248
	v_med3_f32 v49, v49, s55, v248
	v_cvt_pk_fp8_f32 v26, v10, v11
	v_cvt_pk_fp8_f32 v27, v40, v41
	v_pk_mul_f32 v[36:37], v[12:13], s[14:15] op_sel_hi:[1,0]
	v_pk_mul_f32 v[16:17], v[16:17], s[14:15] op_sel_hi:[1,0]
	v_pk_fma_f32 v[60:61], v[168:169], s[16:17], v[38:39] op_sel_hi:[1,0,1]
	v_pk_fma_f32 v[66:67], v[164:165], s[16:17], v[14:15] op_sel_hi:[1,0,1]
	v_med3_f32 v52, v52, s55, v248
	v_med3_f32 v53, v53, s55, v248
	v_med3_f32 v56, v56, s55, v248
	v_med3_f32 v57, v57, s55, v248
	v_cvt_pk_fp8_f32 v28, v44, v45
	v_cvt_pk_fp8_f32 v29, v48, v49
	v_pk_fma_f32 v[2:3], v[194:195], s[16:17], v[36:37] op_sel_hi:[1,0,1]
	v_pk_fma_f32 v[12:13], v[190:191], s[16:17], v[16:17] op_sel_hi:[1,0,1]
	v_med3_f32 v60, v60, s55, v248
	v_med3_f32 v61, v61, s55, v248
	v_med3_f32 v65, v66, s55, v248
	v_med3_f32 v66, v67, s55, v248
	v_cvt_pk_fp8_f32 v30, v52, v53
	v_cvt_pk_fp8_f32 v31, v56, v57
	v_pk_fma_f32 v[42:43], v[186:187], s[16:17], v[36:37] op_sel_hi:[1,0,1]
	v_pk_fma_f32 v[46:47], v[182:183], s[16:17], v[16:17] op_sel_hi:[1,0,1]
	v_med3_f32 v2, v2, s55, v248
	v_med3_f32 v3, v3, s55, v248
	v_med3_f32 v12, v12, s55, v248
	v_med3_f32 v13, v13, s55, v248
	v_cvt_pk_fp8_f32 v32, v60, v61
	v_cvt_pk_fp8_f32 v33, v65, v66
	v_pk_fma_f32 v[50:51], v[178:179], s[16:17], v[36:37] op_sel_hi:[1,0,1]
	v_pk_fma_f32 v[54:55], v[174:175], s[16:17], v[16:17] op_sel_hi:[1,0,1]
	v_med3_f32 v42, v42, s55, v248
	v_med3_f32 v43, v43, s55, v248
	v_med3_f32 v46, v46, s55, v248
	v_med3_f32 v47, v47, s55, v248
	v_cvt_pk_fp8_f32 v26, v2, v3 op_sel:[0,0,1]
	v_cvt_pk_fp8_f32 v27, v12, v13 op_sel:[0,0,1]
	v_pk_fma_f32 v[58:59], v[170:171], s[16:17], v[36:37] op_sel_hi:[1,0,1]
	v_pk_fma_f32 v[62:63], v[166:167], s[16:17], v[16:17] op_sel_hi:[1,0,1]
	v_med3_f32 v50, v50, s55, v248
	v_med3_f32 v51, v51, s55, v248
	v_med3_f32 v54, v54, s55, v248
	v_med3_f32 v55, v55, s55, v248
	v_cvt_pk_fp8_f32 v28, v42, v43 op_sel:[0,0,1]
	v_cvt_pk_fp8_f32 v29, v46, v47 op_sel:[0,0,1]
	v_med3_f32 v58, v58, s55, v248
	v_med3_f32 v59, v59, s55, v248
	v_med3_f32 v62, v62, s55, v248
	v_med3_f32 v63, v63, s55, v248
	v_cvt_pk_fp8_f32 v30, v50, v51 op_sel:[0,0,1]
	v_cvt_pk_fp8_f32 v31, v54, v55 op_sel:[0,0,1]
	v_cvt_pk_fp8_f32 v32, v58, v59 op_sel:[0,0,1]
	v_cvt_pk_fp8_f32 v33, v62, v63 op_sel:[0,0,1]
	v_pk_fma_f32 v[10:11], v[160:161], s[16:17], v[38:39] op_sel_hi:[1,0,1]
	global_store_dwordx2 v[4:5], v[26:27], off
	global_store_dwordx2 v[6:7], v[28:29], off
	global_store_dwordx2 v[8:9], v[30:31], off
	v_pk_fma_f32 v[28:29], v[156:157], s[16:17], v[14:15] op_sel_hi:[1,0,1]
	v_med3_f32 v30, v10, s55, v248
	v_med3_f32 v11, v11, s55, v248
	v_mov_b32_e32 v10, 0
	v_cvt_pk_fp8_f32 v10, v30, v11
	v_med3_f32 v28, v28, s55, v248
	v_med3_f32 v29, v29, s55, v248
	v_mov_b32_e32 v11, 0
	v_lshl_add_u64 v[26:27], v[34:35], 0, v[0:1]
	v_cvt_pk_fp8_f32 v11, v28, v29
	v_pk_fma_f32 v[28:29], v[152:153], s[16:17], v[38:39] op_sel_hi:[1,0,1]
	global_store_dwordx2 v[26:27], v[32:33], off
	v_pk_fma_f32 v[32:33], v[148:149], s[16:17], v[14:15] op_sel_hi:[1,0,1]
	v_med3_f32 v34, v28, s55, v248
	v_med3_f32 v29, v29, s55, v248
	v_mov_b32_e32 v28, 0
	v_pk_fma_f32 v[2:3], v[162:163], s[16:17], v[36:37] op_sel_hi:[1,0,1]
	v_cvt_pk_fp8_f32 v28, v34, v29
	v_med3_f32 v32, v32, s55, v248
	v_med3_f32 v33, v33, s55, v248
	v_mov_b32_e32 v29, 0
	v_pk_fma_f32 v[12:13], v[158:159], s[16:17], v[16:17] op_sel_hi:[1,0,1]
;     __device__ __forceinline__ void operator()(const f32x4 (&acc)[2][2][4][2], const Unit& u, int wr, int wc, int fr, int fq) const {
;     ...
;         for (int bj = 0; bj < 2; ++bj) { const int c0 = u.pn * 256 + bj * 128 + wc * 32 + 8 * fq; const f32x4 b0 = bq[bj][0] * Y8_SCALE, b1 = bq[bj][1] * Y8_SCALE;
; #pragma unroll
;             for (int ai = 0; ai < 2; ++ai)
; #pragma unroll
;                 for (int m = 0; m < 4; ++m) { const int r = row0 + ai * 128 + m * 16; const f32x4 v0 = acc[ai][bj][m][0] * (W8_INV * Y8_SCALE) + b0, v1 = acc[ai][bj][m][1] * (W8_INV * Y8_SCALE) + b1; v2u w;
;                     w.x = pk4_fp8(v0[0], v0[1], v0[2], v0[3]); w.y = pk4_fp8(v1[0], v1[1], v1[2], v1[3]);
;                     *(v2u*)(YK + ((size_t)u.z * 256 + r) * D + c0) = w; } }
	v_med3_f32 v2, v2, s55, v248
	v_med3_f32 v3, v3, s55, v248
	v_cvt_pk_fp8_f32 v29, v32, v33
	v_cvt_pk_fp8_f32 v10, v2, v3 op_sel:[0,0,1]
	v_med3_f32 v2, v12, s55, v248
	v_med3_f32 v3, v13, s55, v248
	v_pk_fma_f32 v[12:13], v[154:155], s[16:17], v[36:37] op_sel_hi:[1,0,1]
	v_cvt_pk_fp8_f32 v11, v2, v3 op_sel:[0,0,1]
	v_pk_fma_f32 v[30:31], v[150:151], s[16:17], v[16:17] op_sel_hi:[1,0,1]
	v_med3_f32 v12, v12, s55, v248
	v_med3_f32 v13, v13, s55, v248
	v_cvt_pk_fp8_f32 v28, v12, v13 op_sel:[0,0,1]
	v_med3_f32 v12, v30, s55, v248
	v_med3_f32 v13, v31, s55, v248
	v_lshl_add_u64 v[2:3], s[4:5], 0, v[212:213]
	v_cvt_pk_fp8_f32 v29, v12, v13 op_sel:[0,0,1]
	v_lshl_add_u64 v[2:3], v[2:3], 0, v[0:1]
	global_store_dwordx2 v[2:3], v[10:11], off
	v_lshl_add_u64 v[10:11], s[4:5], 0, v[214:215]
	v_lshl_add_u64 v[10:11], v[10:11], 0, v[0:1]
	global_store_dwordx2 v[10:11], v[28:29], off
	v_pk_fma_f32 v[28:29], v[144:145], s[16:17], v[38:39] op_sel_hi:[1,0,1]
	v_pk_fma_f32 v[32:33], v[140:141], s[16:17], v[14:15] op_sel_hi:[1,0,1]
	v_med3_f32 v34, v28, s55, v248
	v_med3_f32 v29, v29, s55, v248
	v_mov_b32_e32 v28, 0
	v_cvt_pk_fp8_f32 v28, v34, v29
	v_med3_f32 v32, v32, s55, v248
	v_med3_f32 v33, v33, s55, v248
	v_mov_b32_e32 v29, 0
	v_cvt_pk_fp8_f32 v29, v32, v33
	v_pk_fma_f32 v[32:33], v[136:137], s[16:17], v[38:39] op_sel_hi:[1,0,1]
	v_pk_fma_f32 v[14:15], v[128:129], s[16:17], v[14:15] op_sel_hi:[1,0,1]
	v_med3_f32 v34, v32, s55, v248
	v_med3_f32 v33, v33, s55, v248
	v_mov_b32_e32 v32, 0
	v_cvt_pk_fp8_f32 v32, v34, v33
	v_med3_f32 v14, v14, s55, v248
	v_med3_f32 v15, v15, s55, v248
	v_mov_b32_e32 v33, 0
	v_pk_fma_f32 v[12:13], v[146:147], s[16:17], v[36:37] op_sel_hi:[1,0,1]
	v_cvt_pk_fp8_f32 v33, v14, v15
	v_pk_fma_f32 v[30:31], v[142:143], s[16:17], v[16:17] op_sel_hi:[1,0,1]
	v_med3_f32 v12, v12, s55, v248
	v_med3_f32 v13, v13, s55, v248
	v_cvt_pk_fp8_f32 v28, v12, v13 op_sel:[0,0,1]
	v_med3_f32 v12, v30, s55, v248
	v_med3_f32 v13, v31, s55, v248
	v_pk_fma_f32 v[30:31], v[138:139], s[16:17], v[36:37] op_sel_hi:[1,0,1]
	v_pk_fma_f32 v[16:17], v[130:131], s[16:17], v[16:17] op_sel_hi:[1,0,1]
	v_med3_f32 v30, v30, s55, v248
	v_med3_f32 v31, v31, s55, v248
	v_med3_f32 v14, v16, s55, v248
	v_med3_f32 v15, v17, s55, v248
	v_cvt_pk_fp8_f32 v32, v30, v31 op_sel:[0,0,1]
	v_cvt_pk_fp8_f32 v33, v14, v15 op_sel:[0,0,1]
	v_cvt_pk_fp8_f32 v29, v12, v13 op_sel:[0,0,1]
	v_lshl_add_u64 v[12:13], s[4:5], 0, v[216:217]
	v_lshl_add_u64 v[14:15], s[4:5], 0, v[218:219]
	v_pk_mul_f32 v[16:17], v[22:23], s[14:15] op_sel_hi:[1,0]
	v_lshl_add_u64 v[12:13], v[12:13], 0, v[0:1]
	v_lshl_add_u64 v[0:1], v[14:15], 0, v[0:1]
	v_pk_mul_f32 v[14:15], v[24:25], s[14:15] op_sel_hi:[1,0]
	v_pk_fma_f32 v[24:25], v[132:133], s[16:17], v[16:17] op_sel_hi:[1,0,1]
	global_store_dwordx2 v[0:1], v[32:33], off
	v_med3_f32 v32, v24, s55, v248
	v_med3_f32 v25, v25, s55, v248
	v_mov_b32_e32 v24, 0
	v_cvt_pk_fp8_f32 v24, v32, v25
	v_pk_mul_f32 v[18:19], v[18:19], s[14:15] op_sel_hi:[1,0]
	v_pk_mul_f32 v[20:21], v[20:21], s[14:15] op_sel_hi:[1,0]
	v_pk_fma_f32 v[22:23], v[134:135], s[16:17], v[14:15] op_sel_hi:[1,0,1]
	v_pk_fma_f32 v[30:31], v[124:125], s[16:17], v[18:19] op_sel_hi:[1,0,1]
	global_store_dwordx2 v[12:13], v[28:29], off
	v_pk_fma_f32 v[28:29], v[126:127], s[16:17], v[20:21] op_sel_hi:[1,0,1]
	v_med3_f32 v22, v22, s55, v248
	v_med3_f32 v23, v23, s55, v248
	v_med3_f32 v30, v30, s55, v248
	v_med3_f32 v31, v31, s55, v248
	v_mov_b32_e32 v25, 0
	v_cvt_pk_fp8_f32 v25, v30, v31
	v_cvt_pk_fp8_f32 v24, v22, v23 op_sel:[0,0,1]
	v_med3_f32 v22, v28, s55, v248
	v_med3_f32 v23, v29, s55, v248
	v_pk_fma_f32 v[28:29], v[120:121], s[16:17], v[16:17] op_sel_hi:[1,0,1]
	v_cvt_pk_fp8_f32 v25, v22, v23 op_sel:[0,0,1]
	v_med3_f32 v34, v28, s55, v248
	v_med3_f32 v29, v29, s55, v248
	v_mov_b32_e32 v28, 0
	v_cvt_pk_fp8_f32 v28, v34, v29
	v_pk_fma_f32 v[22:23], v[122:123], s[16:17], v[14:15] op_sel_hi:[1,0,1]
	v_pk_fma_f32 v[32:33], v[116:117], s[16:17], v[18:19] op_sel_hi:[1,0,1]
	v_pk_fma_f32 v[30:31], v[118:119], s[16:17], v[20:21] op_sel_hi:[1,0,1]
	v_med3_f32 v22, v22, s55, v248
	v_med3_f32 v23, v23, s55, v248
	v_med3_f32 v32, v32, s55, v248
	v_med3_f32 v33, v33, s55, v248
	v_mov_b32_e32 v29, 0
	v_cvt_pk_fp8_f32 v29, v32, v33
	v_cvt_pk_fp8_f32 v28, v22, v23 op_sel:[0,0,1]
	v_med3_f32 v22, v30, s55, v248
	v_med3_f32 v23, v31, s55, v248
	v_pk_fma_f32 v[30:31], v[112:113], s[16:17], v[16:17] op_sel_hi:[1,0,1]
	v_cvt_pk_fp8_f32 v29, v22, v23 op_sel:[0,0,1]
	v_med3_f32 v36, v30, s55, v248
	v_med3_f32 v31, v31, s55, v248
	v_mov_b32_e32 v30, 0
	v_cvt_pk_fp8_f32 v30, v36, v31
	v_pk_fma_f32 v[22:23], v[114:115], s[16:17], v[14:15] op_sel_hi:[1,0,1]
; #define PG8_BAR __builtin_amdgcn_s_barrier()
;     __device__ __forceinline__ void done(const Unit& u) const { if (u.pm == (c & 7)) convert_share(); }
; template <class Epi, class Sched, bool ALIGN_EPI = false, bool SP2 = false>
; __device__ __forceinline__ void gemm_phase(PG8_LAS unsigned char* lds, const Geo geo, const Sched& S, const Epi& E, const int wave_) {
;     ...
;         if constexpr (!Epi::AFTER_DRAIN) { E(acc, cur, wr, wc, fr, fq); S.done(cur); }
;         if (!has_next) break;
; #pragma unroll
;         for (int a = 0; a < 2; ++a)
; #pragma unroll
;             for (int b = 0; b < 2; ++b)
; #pragma unroll
;                 for (int m = 0; m < 4; ++m)
; #pragma unroll
;                     for (int n = 0; n < 2; ++n) acc[a][b][m][n] = (f32x4){0.f, 0.f, 0.f, 0.f};
;         cur = nxt; cA = nA; cB = nB; ++ui;
; #pragma unroll
;         for (int i = 0; i < 2; ++i) { c0[i] = n0[i]; c1[i] = n1[i]; }
;         if constexpr (ALIGN_EPI) { if (wr == 1) PG8_BAR; }
;     __device__ __forceinline__ void operator()(const f32x4 (&acc)[2][2][4][2], const Unit& u, int wr, int wc, int fr, int fq) const {
;     ...
;         for (int bj = 0; bj < 2; ++bj) { const int c0 = u.pn * 256 + bj * 128 + wc * 32 + 8 * fq; const f32x4 b0 = bq[bj][0] * Y8_SCALE, b1 = bq[bj][1] * Y8_SCALE;
; #pragma unroll
;             for (int ai = 0; ai < 2; ++ai)
; #pragma unroll
;                 for (int m = 0; m < 4; ++m) { const int r = row0 + ai * 128 + m * 16; const f32x4 v0 = acc[ai][bj][m][0] * (W8_INV * Y8_SCALE) + b0, v1 = acc[ai][bj][m][1] * (W8_INV * Y8_SCALE) + b1; v2u w;
;                     w.x = pk4_fp8(v0[0], v0[1], v0[2], v0[3]); w.y = pk4_fp8(v1[0], v1[1], v1[2], v1[3]);
;                     *(v2u*)(YK + ((size_t)u.z * 256 + r) * D + c0) = w; } }
	v_pk_fma_f32 v[34:35], v[108:109], s[16:17], v[18:19] op_sel_hi:[1,0,1]
	v_pk_fma_f32 v[32:33], v[110:111], s[16:17], v[20:21] op_sel_hi:[1,0,1]
	v_med3_f32 v22, v22, s55, v248
	v_med3_f32 v23, v23, s55, v248
	v_med3_f32 v34, v34, s55, v248
	v_med3_f32 v35, v35, s55, v248
	v_mov_b32_e32 v31, 0
	v_cvt_pk_fp8_f32 v31, v34, v35
	v_cvt_pk_fp8_f32 v30, v22, v23 op_sel:[0,0,1]
	v_med3_f32 v22, v32, s55, v248
	v_med3_f32 v23, v33, s55, v248
	v_pk_fma_f32 v[32:33], v[104:105], s[16:17], v[16:17] op_sel_hi:[1,0,1]
	v_pk_fma_f32 v[36:37], v[100:101], s[16:17], v[18:19] op_sel_hi:[1,0,1]
	v_med3_f32 v38, v32, s55, v248
	v_med3_f32 v33, v33, s55, v248
	v_mov_b32_e32 v32, 0
	v_cvt_pk_fp8_f32 v32, v38, v33
	v_med3_f32 v36, v36, s55, v248
	v_med3_f32 v37, v37, s55, v248
	v_mov_b32_e32 v33, 0
	v_cvt_pk_fp8_f32 v33, v36, v37
	v_cvt_pk_fp8_f32 v31, v22, v23 op_sel:[0,0,1]
	v_pk_fma_f32 v[22:23], v[106:107], s[16:17], v[14:15] op_sel_hi:[1,0,1]
	v_pk_fma_f32 v[34:35], v[102:103], s[16:17], v[20:21] op_sel_hi:[1,0,1]
	v_med3_f32 v22, v22, s55, v248
	v_med3_f32 v23, v23, s55, v248
	v_cvt_pk_fp8_f32 v32, v22, v23 op_sel:[0,0,1]
	v_med3_f32 v22, v34, s55, v248
	v_med3_f32 v23, v35, s55, v248
	v_cvt_pk_fp8_f32 v33, v22, v23 op_sel:[0,0,1]
	global_store_dwordx2 v[4:5], v[24:25], off offset:128
	global_store_dwordx2 v[6:7], v[28:29], off offset:128
	global_store_dwordx2 v[8:9], v[30:31], off offset:128
	global_store_dwordx2 v[26:27], v[32:33], off offset:128
	v_pk_fma_f32 v[6:7], v[96:97], s[16:17], v[16:17] op_sel_hi:[1,0,1]
	v_pk_fma_f32 v[4:5], v[98:99], s[16:17], v[14:15] op_sel_hi:[1,0,1]
	v_med3_f32 v24, v6, s55, v248
	v_med3_f32 v7, v7, s55, v248
	v_mov_b32_e32 v6, 0
	v_cvt_pk_fp8_f32 v6, v24, v7
	v_pk_fma_f32 v[22:23], v[92:93], s[16:17], v[18:19] op_sel_hi:[1,0,1]
	v_pk_fma_f32 v[8:9], v[94:95], s[16:17], v[20:21] op_sel_hi:[1,0,1]
	v_med3_f32 v4, v4, s55, v248
	v_med3_f32 v5, v5, s55, v248
	v_med3_f32 v22, v22, s55, v248
	v_med3_f32 v23, v23, s55, v248
	v_mov_b32_e32 v7, 0
	v_cvt_pk_fp8_f32 v7, v22, v23
	v_cvt_pk_fp8_f32 v6, v4, v5 op_sel:[0,0,1]
	v_med3_f32 v4, v8, s55, v248
	v_med3_f32 v5, v9, s55, v248
	v_pk_fma_f32 v[8:9], v[88:89], s[16:17], v[16:17] op_sel_hi:[1,0,1]
	v_cvt_pk_fp8_f32 v7, v4, v5 op_sel:[0,0,1]
	v_med3_f32 v26, v8, s55, v248
	v_med3_f32 v9, v9, s55, v248
	v_mov_b32_e32 v8, 0
	v_cvt_pk_fp8_f32 v8, v26, v9
	v_pk_fma_f32 v[4:5], v[90:91], s[16:17], v[14:15] op_sel_hi:[1,0,1]
	v_pk_fma_f32 v[24:25], v[84:85], s[16:17], v[18:19] op_sel_hi:[1,0,1]
	v_pk_fma_f32 v[22:23], v[86:87], s[16:17], v[20:21] op_sel_hi:[1,0,1]
	v_med3_f32 v4, v4, s55, v248
	v_med3_f32 v5, v5, s55, v248
	v_med3_f32 v24, v24, s55, v248
	v_med3_f32 v25, v25, s55, v248
	v_mov_b32_e32 v9, 0
	v_cvt_pk_fp8_f32 v9, v24, v25
	v_cvt_pk_fp8_f32 v8, v4, v5 op_sel:[0,0,1]
	v_med3_f32 v4, v22, s55, v248
	v_med3_f32 v5, v23, s55, v248
	v_pk_fma_f32 v[22:23], v[80:81], s[16:17], v[16:17] op_sel_hi:[1,0,1]
	v_pk_fma_f32 v[26:27], v[76:77], s[16:17], v[18:19] op_sel_hi:[1,0,1]
	v_med3_f32 v28, v22, s55, v248
	v_med3_f32 v23, v23, s55, v248
	v_mov_b32_e32 v22, 0
	v_cvt_pk_fp8_f32 v22, v28, v23
	v_med3_f32 v26, v26, s55, v248
	v_med3_f32 v27, v27, s55, v248
	v_mov_b32_e32 v23, 0
	v_cvt_pk_fp8_f32 v23, v26, v27
	v_cvt_pk_fp8_f32 v9, v4, v5 op_sel:[0,0,1]
	v_pk_fma_f32 v[4:5], v[82:83], s[16:17], v[14:15] op_sel_hi:[1,0,1]
	v_pk_fma_f32 v[24:25], v[78:79], s[16:17], v[20:21] op_sel_hi:[1,0,1]
	v_med3_f32 v4, v4, s55, v248
	v_med3_f32 v5, v5, s55, v248
	v_cvt_pk_fp8_f32 v22, v4, v5 op_sel:[0,0,1]
	v_med3_f32 v4, v24, s55, v248
	v_med3_f32 v5, v25, s55, v248
	v_cvt_pk_fp8_f32 v23, v4, v5 op_sel:[0,0,1]
	v_pk_fma_f32 v[4:5], v[74:75], s[16:17], v[14:15] op_sel_hi:[1,0,1]
	v_pk_fma_f32 v[14:15], v[72:73], s[16:17], v[16:17] op_sel_hi:[1,0,1]
	v_pk_fma_f32 v[16:17], v[70:71], s[16:17], v[20:21] op_sel_hi:[1,0,1]
	v_pk_fma_f32 v[18:19], v[68:69], s[16:17], v[18:19] op_sel_hi:[1,0,1]
	v_med3_f32 v20, v14, s55, v248
	v_med3_f32 v15, v15, s55, v248
	v_mov_b32_e32 v14, 0
	v_cvt_pk_fp8_f32 v14, v20, v15
	v_med3_f32 v18, v18, s55, v248
	v_med3_f32 v19, v19, s55, v248
	v_mov_b32_e32 v15, 0
	v_cvt_pk_fp8_f32 v15, v18, v19
	v_med3_f32 v4, v4, s55, v248
	v_med3_f32 v5, v5, s55, v248
	v_cvt_pk_fp8_f32 v14, v4, v5 op_sel:[0,0,1]
	v_med3_f32 v4, v16, s55, v248
	v_med3_f32 v5, v17, s55, v248
	v_cvt_pk_fp8_f32 v15, v4, v5 op_sel:[0,0,1]
	global_store_dwordx2 v[2:3], v[6:7], off offset:128
	global_store_dwordx2 v[10:11], v[8:9], off offset:128
	global_store_dwordx2 v[12:13], v[22:23], off offset:128
	global_store_dwordx2 v[0:1], v[14:15], off offset:128
	s_cbranch_vccnz .LBB0_1610
	s_andn2_b64 vcc, exec, s[8:9]
	s_cbranch_vccnz .LBB0_1609
	s_barrier
	s_branch .LBB0_1609
